# edge1 XCD runs of 8 workgroups (was 16)
# baseline (speedup 1.0000x reference)
.LBB4_4:
	s_or_b64 exec, exec, s[6:7]
	s_and_b32 s86, s2, 7
	s_lshl_b32 s86, s86, 3
	s_bfe_u32 s87, s2, 0x30003
	s_or_b32 s86, s86, s87
	s_and_b32 s87, s2, 0xffffffc0
	s_or_b32 s2, s86, s87
	v_lshl_or_b32 v64, s2, 2, v48
	v_min_i32_e32 v48, 0x61a7, v64
	v_lshl_or_b32 v54, v48, 5, v66
	v_ashrrev_i32_e32 v55, 31, v54
	v_lshl_add_u64 v[56:57], v[54:55], 4, s[8:9]
	v_max_i32_e32 v48, 1, v54
	v_mov_b32_e32 v49, 0
	v_lshl_add_u64 v[58:59], v[48:49], 4, s[8:9]
	global_load_dwordx4 v[48:51], v[56:57], off
	global_load_dword v80, v[56:57], off offset:24
	global_load_dword v55, v[58:59], off offset:-8
	s_load_dword s10, s[0:1], 0x48
	s_waitcnt vmcnt(13)
	ds_write_b128 v46, v[14:17] offset:12800
	s_waitcnt vmcnt(12)
	ds_write_b128 v46, v[22:25] offset:16896
	s_waitcnt vmcnt(10)
	ds_write_b128 v46, v[42:45] offset:20992
	s_waitcnt vmcnt(9)
	v_cvt_f16_f32_e32 v14, v34
	v_cvt_f16_f32_e32 v15, v37
	v_cvt_pk_f16_f32 v17, v35, v36
	s_waitcnt vmcnt(8)
	v_cvt_f16_f32_e32 v23, v41
	v_pack_b32_f16 v16, v14, v17
	v_alignbit_b32 v17, v15, v17, 16
	v_cvt_f16_f32_e32 v15, v38
	v_cvt_pk_f16_f32 v24, v39, v40
	v_lshlrev_b32_e32 v14, 3, v0
	v_alignbit_b32 v23, v23, v24, 16
	v_pack_b32_f16 v22, v15, v24
	s_waitcnt vmcnt(7)
	v_cvt_f16_f32_e32 v15, v18
	ds_write2st64_b64 v14, v[16:17], v[22:23] offset1:4
	v_cvt_pk_f16_f32 v17, v19, v20
	v_cvt_f16_f32_e32 v18, v21
	v_pack_b32_f16 v16, v15, v17
	s_waitcnt vmcnt(6)
	v_cvt_f16_f32_e32 v15, v26
	v_cvt_f16_f32_e32 v19, v29
	s_waitcnt vmcnt(5)
	v_cvt_f16_f32_e32 v6, v6
	v_cvt_pk_f16_f32 v7, v7, v8
	v_cvt_f16_f32_e32 v8, v9
	s_waitcnt vmcnt(4)
	v_cvt_f16_f32_e32 v9, v10
	v_cvt_f16_f32_e32 v10, v13
	v_cvt_pk_f16_f32 v20, v27, v28
	v_cvt_pk_f16_f32 v11, v11, v12
	v_alignbit_b32 v17, v18, v17, 16
	v_pack_b32_f16 v18, v15, v20
	v_alignbit_b32 v19, v19, v20, 16
	v_pack_b32_f16 v6, v6, v7
	v_alignbit_b32 v7, v8, v7, 16
	v_pack_b32_f16 v8, v9, v11
	v_alignbit_b32 v9, v10, v11, 16
	ds_write_b128 v46, v[30:33] offset:25088
	ds_write2st64_b64 v14, v[16:17], v[18:19] offset0:8 offset1:12
	ds_write2st64_b64 v14, v[6:7], v[8:9] offset0:16 offset1:20
	s_and_saveexec_b64 s[2:3], vcc
	s_cbranch_execnz .LBB4_74
	s_or_b64 exec, exec, s[2:3]
	s_and_saveexec_b64 s[2:3], vcc
	s_cbranch_execnz .LBB4_75
